# speedup vs baseline: 1.0025x; 1.0025x over previous
.LBB3_7:
	s_waitcnt lgkmcnt(14)
	v_mfma_f32_32x32x16_bf16 v[2:17], v[142:145], v[162:165], v[2:17]
	v_exp_f32_e32 v82, v82
	v_exp_f32_e32 v83, v83
	v_exp_f32_e32 v84, v84
	v_exp_f32_e32 v85, v85
	s_waitcnt lgkmcnt(12)
	v_mfma_f32_32x32x16_bf16 v[18:33], v[142:145], v[170:173], v[18:33]
	v_exp_f32_e32 v86, v86
	v_exp_f32_e32 v87, v87
	v_exp_f32_e32 v88, v88
	v_exp_f32_e32 v89, v89
	v_add_u32_e32 v110, s40, v215
	ds_read_b128 v[190:193], v110
	ds_read_b128 v[186:189], v110 offset:512
	s_waitcnt lgkmcnt(12)
	v_mfma_f32_32x32x16_bf16 v[2:17], v[138:141], v[166:169], v[2:17]
	v_exp_f32_e32 v90, v90
	v_exp_f32_e32 v91, v91
	v_exp_f32_e32 v92, v92
	v_exp_f32_e32 v93, v93
	ds_read_b128 v[182:185], v110 offset:2048
	ds_read_b128 v[178:181], v110 offset:2560
	s_waitcnt lgkmcnt(12)
	v_mfma_f32_32x32x16_bf16 v[18:33], v[138:141], v[118:121], v[18:33]
	v_exp_f32_e32 v94, v94
	v_exp_f32_e32 v95, v95
	v_exp_f32_e32 v96, v96
	v_exp_f32_e32 v97, v97
	ds_read_b128 v[174:177], v110 offset:4096
	ds_read_b128 v[170:173], v110 offset:4608
	s_waitcnt lgkmcnt(12)
	v_mfma_f32_32x32x16_bf16 v[2:17], v[134:137], v[114:117], v[2:17]
	v_exp_f32_e32 v66, v66
	v_exp_f32_e32 v67, v67
	v_exp_f32_e32 v68, v68
	v_exp_f32_e32 v69, v69
	ds_read_b128 v[166:169], v110 offset:6144
	ds_read_b128 v[162:165], v110 offset:6656
	s_waitcnt lgkmcnt(12)
	v_mfma_f32_32x32x16_bf16 v[18:33], v[134:137], v[98:101], v[18:33]
	v_exp_f32_e32 v70, v70
	v_exp_f32_e32 v71, v71
	v_exp_f32_e32 v72, v72
	v_exp_f32_e32 v73, v73
	s_waitcnt lgkmcnt(10)
	v_mfma_f32_32x32x16_bf16 v[2:17], v[130:133], v[102:105], v[2:17]
	v_exp_f32_e32 v74, v74
	v_exp_f32_e32 v75, v75
	v_exp_f32_e32 v76, v76
	v_exp_f32_e32 v77, v77
	s_waitcnt lgkmcnt(8)
	v_mfma_f32_32x32x16_bf16 v[18:33], v[130:133], v[106:109], v[18:33]
	v_exp_f32_e32 v78, v78
	v_exp_f32_e32 v79, v79
	v_exp_f32_e32 v80, v80
	v_exp_f32_e32 v81, v81
	s_add_i32 s11, s11, 2
	v_lshl_add_u64 v[204:205], v[204:205], 0, s[22:23]
	s_waitcnt vmcnt(2) lgkmcnt(0)
	s_barrier
	s_andn2_b64 vcc, exec, s[26:27]
	s_cbranch_vccnz .LBB3_9
	v_add_u32_e32 v110, s37, v200
	ds_read_b128 v[98:101], v110 offset:49248
	ds_read_b128 v[102:105], v110 offset:49216
	ds_read_b128 v[106:109], v110 offset:49152
	ds_read_b128 v[110:113], v110 offset:49184
	s_waitcnt lgkmcnt(3)
	v_pk_mul_f32 v[16:17], v[16:17], v[100:101]
	v_pk_mul_f32 v[14:15], v[14:15], v[98:99]
	s_waitcnt lgkmcnt(2)
	v_pk_mul_f32 v[12:13], v[12:13], v[104:105]
	v_pk_mul_f32 v[10:11], v[10:11], v[102:103]
	s_waitcnt lgkmcnt(0)
	v_pk_mul_f32 v[8:9], v[8:9], v[112:113]
	v_pk_mul_f32 v[6:7], v[6:7], v[110:111]
	v_pk_mul_f32 v[4:5], v[4:5], v[108:109]
	v_pk_mul_f32 v[2:3], v[2:3], v[106:107]
	v_pk_mul_f32 v[32:33], v[32:33], v[100:101]
	v_pk_mul_f32 v[30:31], v[30:31], v[98:99]
	v_pk_mul_f32 v[28:29], v[28:29], v[104:105]
	v_pk_mul_f32 v[26:27], v[26:27], v[102:103]
	v_pk_mul_f32 v[24:25], v[24:25], v[112:113]
	v_pk_mul_f32 v[22:23], v[22:23], v[110:111]
	v_pk_mul_f32 v[20:21], v[20:21], v[108:109]
	v_pk_mul_f32 v[18:19], v[18:19], v[106:107]
.LBB3_9:
	s_add_i32 s26, s40, 0x2000
	s_cmpk_lg_i32 s40, 0x4000
	s_cselect_b32 s26, s26, 0
	s_cmp_lt_u32 s11, 25
	s_cbranch_scc0 .LBB3_17
	v_mov_b64_e32 v[208:209], v[206:207]
	s_mov_b32 s27, s38
	s_mov_b32 s39, s40
	s_mov_b32 s38, s26
	s_branch .LBB3_2
